# speedup vs baseline: 1.0033x; 1.0033x over previous
.Lm_steps:
	s_waitcnt lgkmcnt(4)
	v_mfma_f32_32x32x16_f16 v[64:79], v[92:95], v[8:11], 0
	ds_read_b128 v[88:91], v128 offset:26624
	s_sub_u32 s30, s28, s25
	ds_read_b128 v[112:115], v128 offset:4096
	s_mul_i32 s30, s30, 6
	ds_read_b128 v[120:123], v128 offset:6144
	s_add_u32 s30, s30, s24
	v_exp_f32_e32 v48, v48
	s_mul_i32 s31, s28, 6
	v_exp_f32_e32 v49, v49
	s_add_u32 s31, s31, s22
	v_exp_f32_e32 v50, v50
	s_cmp_lt_u32 s28, s25
	v_exp_f32_e32 v51, v51
	s_cselect_b32 s30, s31, s30
	v_exp_f32_e32 v52, v52
	s_lshl_b32 s33, s18, 10
	v_exp_f32_e32 v53, v53
	s_lshl_b32 s31, s30, 12
	v_exp_f32_e32 v54, v54
	s_add_u32 s31, s31, s33
	v_exp_f32_e32 v55, v55
	s_add_u32 s50, s8, s31
	v_cvt_pk_bf16_f32 v80, v48, v49
	s_addc_u32 s51, s9, 0
	v_cvt_pk_bf16_f32 v81, v50, v51
	s_add_u32 s52, s50, 0x3000
	v_cvt_pk_bf16_f32 v82, v52, v53
	s_addc_u32 s53, s51, 0
	v_cvt_pk_bf16_f32 v83, v54, v55
	s_lshl_b32 s31, s30, 10
	ds_read_b128 v[116:119], v128 offset:5120
	s_add_u32 s31, s31, s33
	ds_read_b128 v[124:127], v128 offset:7168
	s_sub_u32 s31, s31, 0
	v_exp_f32_e32 v56, v56
	s_add_u32 s54, s4, s31
	v_exp_f32_e32 v57, v57
	s_addc_u32 s55, s5, 0
	v_exp_f32_e32 v58, v58
	s_add_u32 s34, s48, s33
	v_exp_f32_e32 v59, v59
	s_add_u32 s35, s34, 0x3000
	s_waitcnt lgkmcnt(7)
	v_mfma_f32_32x32x16_bf16 v[16:31], v[96:99], v[80:83], v[16:31]
	s_add_u32 s36, s34, 24576
	v_exp_f32_e32 v60, v60
	v_exp_f32_e32 v61, v61
	v_exp_f32_e32 v62, v62
	v_exp_f32_e32 v63, v63
	v_mfma_f32_32x32x16_bf16 v[32:47], v[104:107], v[80:83], v[32:47]
	v_cvt_pk_bf16_f32 v84, v56, v57
	v_cvt_pk_bf16_f32 v85, v58, v59
	v_cvt_pk_bf16_f32 v86, v60, v61
	v_cvt_pk_bf16_f32 v87, v62, v63
.Lm_after0:
	s_cmp_lt_u32 s28, 9
	s_cbranch_scc0 .Lm_nod_lp
	s_mov_b32 m0, s34
	s_nop 0
	global_load_lds_dwordx4 v2, s[50:51]
.Lm_nod_lp:
.Lm_steps1:
	s_waitcnt lgkmcnt(4)
	v_mfma_f32_32x32x16_f16 v[48:63], v[88:91], v[8:11], 0
	ds_read_b128 v[92:95], v128 offset:27648
	ds_read_b128 v[96:99], v128 offset:8192
	ds_read_b128 v[104:107], v128 offset:10240
	v_exp_f32_e32 v64, v64
	v_exp_f32_e32 v65, v65
	v_exp_f32_e32 v66, v66
	v_exp_f32_e32 v67, v67
	v_mfma_f32_32x32x16_bf16 v[16:31], v[100:103], v[84:87], v[16:31]
	v_exp_f32_e32 v68, v68
	v_exp_f32_e32 v69, v69
	v_exp_f32_e32 v70, v70
	v_exp_f32_e32 v71, v71
	v_mfma_f32_32x32x16_bf16 v[32:47], v[108:111], v[84:87], v[32:47]
	v_cvt_pk_bf16_f32 v80, v64, v65
	v_cvt_pk_bf16_f32 v81, v66, v67
	v_cvt_pk_bf16_f32 v82, v68, v69
	v_cvt_pk_bf16_f32 v83, v70, v71
	ds_read_b128 v[100:103], v128 offset:9216
	ds_read_b128 v[108:111], v128 offset:11264
	v_exp_f32_e32 v72, v72
	v_exp_f32_e32 v73, v73
	v_exp_f32_e32 v74, v74
	v_exp_f32_e32 v75, v75
	s_waitcnt lgkmcnt(7)
	v_mfma_f32_32x32x16_bf16 v[16:31], v[112:115], v[80:83], v[16:31]
	v_exp_f32_e32 v76, v76
	v_exp_f32_e32 v77, v77
	v_exp_f32_e32 v78, v78
	v_exp_f32_e32 v79, v79
	v_mfma_f32_32x32x16_bf16 v[32:47], v[120:123], v[80:83], v[32:47]
	v_cvt_pk_bf16_f32 v84, v72, v73
	v_cvt_pk_bf16_f32 v85, v74, v75
	v_cvt_pk_bf16_f32 v86, v76, v77
	v_cvt_pk_bf16_f32 v87, v78, v79
	s_cmp_lt_u32 s28, 9
	s_cbranch_scc0 .Lm_nod_lq
	s_cmp_eq_u32 s27, 0
	s_cbranch_scc1 .Lm_nod_lq
	s_mov_b32 m0, s35
	s_nop 0
	global_load_lds_dwordx4 v2, s[52:53]
.Lm_nod_lq:
	s_waitcnt lgkmcnt(4)
	v_mfma_f32_32x32x16_f16 v[64:79], v[92:95], v[8:11], 0
	ds_read_b128 v[88:91], v128 offset:28672
	ds_read_b128 v[112:115], v128 offset:12288
	ds_read_b128 v[120:123], v128 offset:14336
	v_exp_f32_e32 v48, v48
	v_exp_f32_e32 v49, v49
	v_exp_f32_e32 v50, v50
	v_exp_f32_e32 v51, v51
	v_mfma_f32_32x32x16_bf16 v[16:31], v[116:119], v[84:87], v[16:31]
	v_exp_f32_e32 v52, v52
	v_exp_f32_e32 v53, v53
	v_exp_f32_e32 v54, v54
	v_exp_f32_e32 v55, v55
	v_mfma_f32_32x32x16_bf16 v[32:47], v[124:127], v[84:87], v[32:47]
	v_cvt_pk_bf16_f32 v80, v48, v49
	v_cvt_pk_bf16_f32 v81, v50, v51
	v_cvt_pk_bf16_f32 v82, v52, v53
	v_cvt_pk_bf16_f32 v83, v54, v55
	ds_read_b128 v[116:119], v128 offset:13312
	ds_read_b128 v[124:127], v128 offset:15360
	v_exp_f32_e32 v56, v56
	v_exp_f32_e32 v57, v57
	v_exp_f32_e32 v58, v58
	v_exp_f32_e32 v59, v59
	s_waitcnt lgkmcnt(7)
	v_mfma_f32_32x32x16_bf16 v[16:31], v[96:99], v[80:83], v[16:31]
	v_exp_f32_e32 v60, v60
	v_exp_f32_e32 v61, v61
	v_exp_f32_e32 v62, v62
	v_exp_f32_e32 v63, v63
	v_mfma_f32_32x32x16_bf16 v[32:47], v[104:107], v[80:83], v[32:47]
	v_cvt_pk_bf16_f32 v84, v56, v57
	v_cvt_pk_bf16_f32 v85, v58, v59
	v_cvt_pk_bf16_f32 v86, v60, v61
	v_cvt_pk_bf16_f32 v87, v62, v63
	s_cmp_lt_u32 s28, 9
	s_cbranch_scc0 .Lm_nod_lr
	s_cmp_eq_u32 s27, 0
	s_cbranch_scc1 .Lm_nod_lr
	s_cmp_lt_u32 s18, 6
	s_cbranch_scc0 .Lm_nod_lr
	s_mov_b32 m0, s36
	s_nop 0
	global_load_lds_dwordx4 v2, s[54:55]
.Lm_nod_lr:
	s_waitcnt lgkmcnt(4)
	v_mfma_f32_32x32x16_f16 v[48:63], v[88:91], v[8:11], 0
	ds_read_b128 v[92:95], v128 offset:29696
	ds_read_b128 v[96:99], v128 offset:16384
	ds_read_b128 v[104:107], v128 offset:18432
	v_exp_f32_e32 v64, v64
	v_exp_f32_e32 v65, v65
	v_exp_f32_e32 v66, v66
	v_exp_f32_e32 v67, v67
	v_mfma_f32_32x32x16_bf16 v[16:31], v[100:103], v[84:87], v[16:31]
	v_exp_f32_e32 v68, v68
	v_exp_f32_e32 v69, v69
	v_exp_f32_e32 v70, v70
	v_exp_f32_e32 v71, v71
	v_mfma_f32_32x32x16_bf16 v[32:47], v[108:111], v[84:87], v[32:47]
	v_cvt_pk_bf16_f32 v80, v64, v65
	v_cvt_pk_bf16_f32 v81, v66, v67
	v_cvt_pk_bf16_f32 v82, v68, v69
	v_cvt_pk_bf16_f32 v83, v70, v71
	ds_read_b128 v[100:103], v128 offset:17408
	ds_read_b128 v[108:111], v128 offset:19456
	v_exp_f32_e32 v72, v72
	v_exp_f32_e32 v73, v73
	v_exp_f32_e32 v74, v74
	v_exp_f32_e32 v75, v75
	s_waitcnt lgkmcnt(7)
	v_mfma_f32_32x32x16_bf16 v[16:31], v[112:115], v[80:83], v[16:31]
	v_exp_f32_e32 v76, v76
	v_exp_f32_e32 v77, v77
	v_exp_f32_e32 v78, v78
	v_exp_f32_e32 v79, v79
	v_mfma_f32_32x32x16_bf16 v[32:47], v[120:123], v[80:83], v[32:47]
	v_cvt_pk_bf16_f32 v84, v72, v73
	v_cvt_pk_bf16_f32 v85, v74, v75
	v_cvt_pk_bf16_f32 v86, v76, v77
	v_cvt_pk_bf16_f32 v87, v78, v79
	s_waitcnt lgkmcnt(4)
	v_mfma_f32_32x32x16_f16 v[64:79], v[92:95], v[8:11], 0
	ds_read_b128 v[88:91], v129 offset:24576
	ds_read_b128 v[112:115], v128 offset:20480
	ds_read_b128 v[120:123], v128 offset:22528
	v_exp_f32_e32 v48, v48
	v_exp_f32_e32 v49, v49
	v_exp_f32_e32 v50, v50
	v_exp_f32_e32 v51, v51
	v_mfma_f32_32x32x16_bf16 v[16:31], v[116:119], v[84:87], v[16:31]
	v_exp_f32_e32 v52, v52
	v_exp_f32_e32 v53, v53
	v_exp_f32_e32 v54, v54
	v_exp_f32_e32 v55, v55
	v_mfma_f32_32x32x16_bf16 v[32:47], v[124:127], v[84:87], v[32:47]
	v_cvt_pk_bf16_f32 v80, v48, v49
	v_cvt_pk_bf16_f32 v81, v50, v51
	v_cvt_pk_bf16_f32 v82, v52, v53
	v_cvt_pk_bf16_f32 v83, v54, v55
	ds_read_b128 v[116:119], v128 offset:21504
	ds_read_b128 v[124:127], v128 offset:23552
	v_exp_f32_e32 v56, v56
	v_exp_f32_e32 v57, v57
	v_exp_f32_e32 v58, v58
	v_exp_f32_e32 v59, v59
	s_waitcnt lgkmcnt(7)
	v_mfma_f32_32x32x16_bf16 v[16:31], v[96:99], v[80:83], v[16:31]
	v_exp_f32_e32 v60, v60
	v_exp_f32_e32 v61, v61
	v_exp_f32_e32 v62, v62
	v_exp_f32_e32 v63, v63
	v_mfma_f32_32x32x16_bf16 v[32:47], v[104:107], v[80:83], v[32:47]
	v_cvt_pk_bf16_f32 v84, v56, v57
	v_cvt_pk_bf16_f32 v85, v58, v59
	v_cvt_pk_bf16_f32 v86, v60, v61
	v_cvt_pk_bf16_f32 v87, v62, v63
	s_waitcnt lgkmcnt(4)
	v_mfma_f32_32x32x16_f16 v[48:63], v[88:91], v[8:11], 0
	ds_read_b128 v[92:95], v129 offset:25600
	ds_read_b128 v[96:99], v129 offset:0
	ds_read_b128 v[104:107], v129 offset:2048
	v_exp_f32_e32 v64, v64
	v_exp_f32_e32 v65, v65
	v_exp_f32_e32 v66, v66
	v_exp_f32_e32 v67, v67
	v_mfma_f32_32x32x16_bf16 v[16:31], v[100:103], v[84:87], v[16:31]
	v_exp_f32_e32 v68, v68
	v_exp_f32_e32 v69, v69
	v_exp_f32_e32 v70, v70
	v_exp_f32_e32 v71, v71
	v_mfma_f32_32x32x16_bf16 v[32:47], v[108:111], v[84:87], v[32:47]
	v_cvt_pk_bf16_f32 v80, v64, v65
	v_cvt_pk_bf16_f32 v81, v66, v67
	v_cvt_pk_bf16_f32 v82, v68, v69
	v_cvt_pk_bf16_f32 v83, v70, v71
	ds_read_b128 v[100:103], v129 offset:1024
	ds_read_b128 v[108:111], v129 offset:3072
	v_exp_f32_e32 v72, v72
	v_exp_f32_e32 v73, v73
	v_exp_f32_e32 v74, v74
	v_exp_f32_e32 v75, v75
	s_waitcnt lgkmcnt(7)
	v_mfma_f32_32x32x16_bf16 v[16:31], v[112:115], v[80:83], v[16:31]
	v_exp_f32_e32 v76, v76
	v_exp_f32_e32 v77, v77
	v_exp_f32_e32 v78, v78
	v_exp_f32_e32 v79, v79
	v_mfma_f32_32x32x16_bf16 v[32:47], v[120:123], v[80:83], v[32:47]
	v_cvt_pk_bf16_f32 v84, v72, v73
	v_cvt_pk_bf16_f32 v85, v74, v75
	v_cvt_pk_bf16_f32 v86, v76, v77
	v_cvt_pk_bf16_f32 v87, v78, v79
	s_waitcnt lgkmcnt(5)
	s_nop 0
	v_mfma_f32_32x32x16_bf16 v[16:31], v[116:119], v[84:87], v[16:31]
	v_mfma_f32_32x32x16_bf16 v[32:47], v[124:127], v[84:87], v[32:47]
	s_mov_b32 s30, s46
	s_mov_b32 s46, s47
	s_mov_b32 s47, s48
	s_mov_b32 s48, s30
	s_add_u32 s27, s27, 1
	s_cmp_lt_u32 s27, 9
	s_cbranch_scc0 .Lm_flush
	s_cmp_eq_u32 s27, s25
	s_cbranch_scc1 .Lm_flush
	s_waitcnt vmcnt(0)
